# P7 epilogue: x rows prefetched one row group ahead (two register sets) and scales one row ahead; P12 g_final hoisted; P2 scale loads batched; moe_tables batched
# baseline (speedup 1.0000x reference)
;     __device__ __forceinline__ void operator()(const f32x4 (&acc)[2][2][4][2], const Unit& u, int wr, int wc, int fr, int fq) const {
;         const int row0 = u.a0 * BM + wr * 64 + fr, col0 = u.a1 * BM + wc * 32 + 4 * fq;
;         const int b = (u.a0 * BM) / SEQ; const float* gt = modf + (size_t)b * NMOD + 2 * D;
;         f32x4 gv[2][2];
; #pragma unroll
;         for (int bj = 0; bj < 2; ++bj)
; #pragma unroll
;             for (int n = 0; n < 2; ++n) gv[bj][n] = *(const f32x4*)(gt + col0 + bj * HALF + n * 16) * *(const f32x4*)(wosc + col0 + bj * HALF + n * 16);
; #pragma unroll
;         for (int ai = 0; ai < 2; ++ai)
; #pragma unroll
;             for (int m = 0; m < 4; ++m) { const int row = row0 + ai * HALF + m * 16; const float sr = asc[row]; const size_t off = (size_t)row * D + col0;
; #pragma unroll
;                 for (int bj = 0; bj < 2; ++bj)
; #pragma unroll
;                     for (int n = 0; n < 2; ++n) { const f32x4 xv = *(const f32x4*)(x + off + bj * HALF + n * 16); const f32x4 r = xv + gv[bj][n] * (__builtin_convertvector(__builtin_bit_cast(i32x4_t, acc[ai][bj][m][n]), f32x4) * sr);
.LBB0_962:
	v_mbcnt_lo_u32_b32 v130, -1, 0
	v_mbcnt_hi_u32_b32 v130, -1, v130
	s_lshl_b32 s2, s67, 8
	s_add_i32 s4, s2, s59
	s_lshl_b32 s2, s68, 8
	v_ashrrev_i32_e32 v128, 2, v130
	s_or_b32 s2, s2, s60
	v_and_b32_e32 v128, -4, v128
	v_add_u32_e32 v132, s2, v128
	s_ashr_i32 s2, s67, 31
	s_lshr_b32 s2, s2, 26
	s_add_i32 s2, s67, s2
	s_ashr_i32 s2, s2, 6
	v_readlane_b32 s68, v254, 2
	s_mul_hi_i32 s3, s2, 0xc000
	s_mul_i32 s2, s2, 0xc000
	v_readlane_b32 s70, v254, 4
	v_readlane_b32 s71, v254, 5
	s_add_u32 s2, s70, s2
	v_ashrrev_i32_e32 v133, 31, v132
	s_addc_u32 s3, s71, s3
	v_lshlrev_b64 v[128:129], 2, v[132:133]
	v_lshl_add_u64 v[166:167], s[2:3], 0, v[128:129]
	v_and_or_b32 v134, v130, 15, s4
	v_lshl_add_u64 v[186:187], s[16:17], 0, v[128:129]
	v_add_co_u32_e32 v128, vcc, s62, v166
	v_ashrrev_i32_e32 v135, 31, v134
	s_nop 0
	v_addc_co_u32_e32 v129, vcc, 0, v167, vcc
	v_lshlrev_b64 v[130:131], 11, v[134:135]
	global_load_dwordx4 v[154:157], v[128:129], off
	global_load_dwordx4 v[158:161], v[186:187], off
	v_lshl_add_u64 v[128:129], v[134:135], 2, s[14:15]
	v_lshl_add_u64 v[130:131], v[130:131], 0, v[132:133]
	global_load_dword v190, v[128:129], off
	v_lshl_add_u64 v[192:193], v[130:131], 2, s[36:37]
	global_load_dwordx4 v[162:165], v[192:193], off
	global_load_dwordx4 v[216:219], v[192:193], off offset:64
	global_load_dwordx4 v[220:223], v[192:193], off offset:512
	global_load_dwordx4 v[224:227], v[192:193], off offset:576
	global_load_dword v248, v[128:129], off offset:64
	v_or_b32_e32 v246, 16, v134
	v_ashrrev_i32_e32 v247, 31, v246
	v_lshlrev_b64 v[246:247], 11, v[246:247]
	v_lshl_add_u64 v[246:247], v[246:247], 0, v[132:133]
	v_lshl_add_u64 v[244:245], v[246:247], 2, s[36:37]
	global_load_dwordx4 v[228:231], v[244:245], off
	global_load_dwordx4 v[232:235], v[244:245], off offset:64
	global_load_dwordx4 v[236:239], v[244:245], off offset:512
	global_load_dwordx4 v[240:243], v[244:245], off offset:576
	v_cvt_f32_i32_e32 v127, v127
	v_cvt_f32_i32_e32 v126, v126
	v_cvt_f32_i32_e32 v125, v125
	v_cvt_f32_i32_e32 v124, v124
	v_lshl_add_u64 v[194:195], v[130:131], 1, s[12:13]
	v_lshl_add_u64 v[182:183], v[166:167], 0, s[20:21]
	global_load_dwordx4 v[166:169], v[186:187], off offset:64
	global_load_dwordx4 v[170:173], v[186:187], off offset:512
	global_load_dwordx4 v[174:177], v[182:183], off offset:64
	global_load_dwordx4 v[178:181], v[182:183], off offset:512
	s_nop 0
	global_load_dwordx4 v[182:185], v[182:183], off offset:576
	s_nop 0
	global_load_dwordx4 v[186:189], v[186:187], off offset:576
	v_cvt_f32_i32_e32 v123, v123
	v_cvt_f32_i32_e32 v121, v121
	v_cvt_f32_i32_e32 v120, v120
	v_cvt_f32_i32_e32 v122, v122
	v_cvt_f32_i32_e32 v119, v119
	v_cvt_f32_i32_e32 v117, v117
	v_cvt_f32_i32_e32 v116, v116
	v_cvt_f32_i32_e32 v118, v118
	v_cvt_f32_i32_e32 v115, v115
	v_cvt_f32_i32_e32 v114, v114
	v_cvt_f32_i32_e32 v113, v113
	v_cvt_f32_i32_e32 v112, v112
	v_cvt_f32_i32_e32 v111, v111
	v_cvt_f32_i32_e32 v109, v109
	v_cvt_f32_i32_e32 v108, v108
	v_cvt_f32_i32_e32 v110, v110
	v_cvt_f32_i32_e32 v107, v107
	v_cvt_f32_i32_e32 v105, v105
	v_cvt_f32_i32_e32 v104, v104
	v_cvt_f32_i32_e32 v106, v106
	v_cvt_f32_i32_e32 v103, v103
	v_cvt_f32_i32_e32 v101, v101
	v_cvt_f32_i32_e32 v100, v100
	v_cvt_f32_i32_e32 v102, v102
	v_cvt_f32_i32_e32 v99, v99
	v_cvt_f32_i32_e32 v98, v98
	v_cvt_f32_i32_e32 v97, v97
	v_cvt_f32_i32_e32 v96, v96
	v_cvt_f32_i32_e32 v95, v95
	v_cvt_f32_i32_e32 v93, v93
	v_cvt_f32_i32_e32 v92, v92
	v_cvt_f32_i32_e32 v94, v94
	v_cvt_f32_i32_e32 v91, v91
	v_cvt_f32_i32_e32 v89, v89
	v_cvt_f32_i32_e32 v88, v88
	v_cvt_f32_i32_e32 v90, v90
	v_cvt_f32_i32_e32 v87, v87
	v_cvt_f32_i32_e32 v85, v85
	v_cvt_f32_i32_e32 v84, v84
	v_cvt_f32_i32_e32 v86, v86
	v_cvt_f32_i32_e32 v83, v83
	v_cvt_f32_i32_e32 v82, v82
	v_cvt_f32_i32_e32 v81, v81
	v_cvt_f32_i32_e32 v80, v80
	v_cvt_f32_i32_e32 v79, v79
	v_cvt_f32_i32_e32 v77, v77
	v_cvt_f32_i32_e32 v76, v76
	v_cvt_f32_i32_e32 v78, v78
	v_cvt_f32_i32_e32 v75, v75
	v_cvt_f32_i32_e32 v73, v73
	v_cvt_f32_i32_e32 v72, v72
	v_cvt_f32_i32_e32 v74, v74
	v_cvt_f32_i32_e32 v71, v71
	v_cvt_f32_i32_e32 v69, v69
	v_cvt_f32_i32_e32 v68, v68
	v_cvt_f32_i32_e32 v70, v70
	v_cvt_f32_i32_e32 v67, v67
	v_cvt_f32_i32_e32 v65, v65
	v_cvt_f32_i32_e32 v64, v64
	v_cvt_f32_i32_e32 v66, v66
	v_cvt_f32_i32_e32 v63, v63
	v_cvt_f32_i32_e32 v61, v61
	v_cvt_f32_i32_e32 v60, v60
	v_cvt_f32_i32_e32 v62, v62
	v_cvt_f32_i32_e32 v59, v59
	v_cvt_f32_i32_e32 v57, v57
	v_cvt_f32_i32_e32 v56, v56
	v_cvt_f32_i32_e32 v58, v58
	v_cvt_f32_i32_e32 v55, v55
	v_cvt_f32_i32_e32 v53, v53
	s_waitcnt vmcnt(15)
	v_pk_mul_f32 v[196:197], v[190:191], v[124:125] op_sel_hi:[0,1]
	v_pk_mul_f32 v[198:199], v[190:191], v[126:127] op_sel_hi:[0,1]
	v_pk_mul_f32 v[124:125], v[156:157], v[160:161]
	v_pk_mul_f32 v[126:127], v[154:155], v[158:159]
	s_waitcnt vmcnt(14)
	v_pk_fma_f32 v[154:155], v[124:125], v[198:199], v[164:165]
	v_pk_fma_f32 v[156:157], v[126:127], v[196:197], v[162:163]
	v_pk_mul_f32 v[158:159], v[190:191], v[120:121] op_sel_hi:[0,1]
	v_cvt_pk_bf16_f32 v156, v156, v157
	v_cvt_pk_bf16_f32 v157, v154, v155
	global_store_dwordx2 v[194:195], v[156:157], off
	v_pk_mul_f32 v[160:161], v[190:191], v[122:123] op_sel_hi:[0,1]
	s_waitcnt vmcnt(4)
	v_pk_mul_f32 v[120:121], v[176:177], v[168:169]
	v_pk_mul_f32 v[122:123], v[174:175], v[166:167]
	v_pk_mul_f32 v[162:163], v[190:191], v[112:113] op_sel_hi:[0,1]
	v_pk_mul_f32 v[164:165], v[190:191], v[114:115] op_sel_hi:[0,1]
	s_waitcnt vmcnt(1)
; DI unsigned pk2(float a, float b) { f32x2 f = {a, b}; bf16x2_t h = __builtin_convertvector(f, bf16x2_t); return __builtin_bit_cast(unsigned, h); }
;     __device__ __forceinline__ void operator()(const f32x4 (&acc)[2][2][4][2], const Unit& u, int wr, int wc, int fr, int fq) const {
;     ...
;         for (int ai = 0; ai < 2; ++ai)
; #pragma unroll
;             for (int m = 0; m < 4; ++m) { const int row = row0 + ai * HALF + m * 16; const float sr = asc[row]; const size_t off = (size_t)row * D + col0;
; #pragma unroll
;                 for (int bj = 0; bj < 2; ++bj)
; #pragma unroll
;                     for (int n = 0; n < 2; ++n) { const f32x4 xv = *(const f32x4*)(x + off + bj * HALF + n * 16); const f32x4 r = xv + gv[bj][n] * (__builtin_convertvector(__builtin_bit_cast(i32x4_t, acc[ai][bj][m][n]), f32x4) * sr);
;                         u32x2 w; w.x = pk2(r[0], r[1]); w.y = pk2(r[2], r[3]); *(u32x2*)(x1 + off + bj * HALF + n * 16) = w; } }
	v_pk_mul_f32 v[112:113], v[184:185], v[188:189]
	v_pk_mul_f32 v[114:115], v[182:183], v[186:187]
	v_cvt_f32_i32_e32 v52, v52
	v_cvt_f32_i32_e32 v54, v54
	v_cvt_f32_i32_e32 v51, v51
	v_cvt_f32_i32_e32 v49, v49
	v_cvt_f32_i32_e32 v48, v48
	v_cvt_f32_i32_e32 v50, v50
	v_cvt_f32_i32_e32 v47, v47
	v_cvt_f32_i32_e32 v45, v45
	v_cvt_f32_i32_e32 v44, v44
	v_cvt_f32_i32_e32 v46, v46
	v_cvt_f32_i32_e32 v43, v43
	v_cvt_f32_i32_e32 v41, v41
	v_cvt_f32_i32_e32 v40, v40
	v_cvt_f32_i32_e32 v42, v42
	v_cvt_f32_i32_e32 v39, v39
	v_cvt_f32_i32_e32 v37, v37
	v_cvt_f32_i32_e32 v36, v36
	v_cvt_f32_i32_e32 v38, v38
	v_cvt_f32_i32_e32 v35, v35
	v_cvt_f32_i32_e32 v33, v33
	v_cvt_f32_i32_e32 v32, v32
	v_cvt_f32_i32_e32 v34, v34
	v_cvt_f32_i32_e32 v31, v31
	v_cvt_f32_i32_e32 v29, v29
	v_cvt_f32_i32_e32 v28, v28
	v_cvt_f32_i32_e32 v30, v30
	v_cvt_f32_i32_e32 v27, v27
	v_cvt_f32_i32_e32 v25, v25
	v_cvt_f32_i32_e32 v24, v24
	v_cvt_f32_i32_e32 v26, v26
	v_cvt_f32_i32_e32 v23, v23
	v_cvt_f32_i32_e32 v21, v21
	v_cvt_f32_i32_e32 v20, v20
	v_cvt_f32_i32_e32 v22, v22
	v_cvt_f32_i32_e32 v19, v19
	v_cvt_f32_i32_e32 v17, v17
	v_cvt_f32_i32_e32 v16, v16
	v_cvt_f32_i32_e32 v18, v18
	v_cvt_f32_i32_e32 v15, v15
	v_cvt_f32_i32_e32 v13, v13
	v_cvt_f32_i32_e32 v12, v12
	v_cvt_f32_i32_e32 v14, v14
	v_cvt_f32_i32_e32 v11, v11
	v_cvt_f32_i32_e32 v9, v9
	v_cvt_f32_i32_e32 v8, v8
	v_cvt_f32_i32_e32 v10, v10
	v_cvt_f32_i32_e32 v7, v7
	v_cvt_f32_i32_e32 v5, v5
	v_cvt_f32_i32_e32 v4, v4
	v_cvt_f32_i32_e32 v6, v6
	v_cvt_f32_i32_e32 v3, v3
	v_cvt_f32_i32_e32 v2, v2
	v_cvt_f32_i32_e32 v1, v1
	v_cvt_f32_i32_e32 v0, v0
	s_andn2_b64 vcc, exec, s[44:45]
	s_mov_b64 s[2:3], -1
	v_readlane_b32 s69, v254, 3
	v_pk_fma_f32 v[156:157], v[120:121], v[160:161], v[218:219]
	v_pk_fma_f32 v[154:155], v[122:123], v[158:159], v[216:217]
	v_pk_mul_f32 v[158:159], v[190:191], v[116:117] op_sel_hi:[0,1]
	v_cvt_pk_bf16_f32 v154, v154, v155
	v_cvt_pk_bf16_f32 v155, v156, v157
	global_store_dwordx2 v[194:195], v[154:155], off offset:32
	v_pk_mul_f32 v[160:161], v[190:191], v[118:119] op_sel_hi:[0,1]
	v_pk_mul_f32 v[116:117], v[180:181], v[172:173]
	v_pk_mul_f32 v[118:119], v[178:179], v[170:171]
	v_pk_fma_f32 v[156:157], v[116:117], v[160:161], v[222:223]
	v_pk_fma_f32 v[154:155], v[118:119], v[158:159], v[220:221]
	v_or_b32_e32 v158, 16, v134
	v_cvt_pk_bf16_f32 v154, v154, v155
	v_cvt_pk_bf16_f32 v155, v156, v157
	global_store_dwordx2 v[194:195], v[154:155], off offset:256
	v_ashrrev_i32_e32 v159, 31, v158
	v_lshl_add_u64 v[160:161], v[158:159], 2, s[14:15]
	v_lshlrev_b64 v[158:159], 11, v[158:159]
	v_lshl_add_u64 v[158:159], v[158:159], 0, v[132:133]
	v_pk_fma_f32 v[156:157], v[112:113], v[164:165], v[226:227]
	v_pk_fma_f32 v[154:155], v[114:115], v[162:163], v[224:225]
	v_lshl_add_u64 v[162:163], v[158:159], 2, s[36:37]
	v_cvt_pk_bf16_f32 v154, v154, v155
	v_cvt_pk_bf16_f32 v155, v156, v157
	global_store_dwordx2 v[194:195], v[154:155], off offset:288
	v_lshl_add_u64 v[158:159], v[158:159], 1, s[12:13]
	global_load_dword v250, v[128:129], off offset:128
	v_or_b32_e32 v246, 32, v134
	v_ashrrev_i32_e32 v247, 31, v246
	v_lshlrev_b64 v[246:247], 11, v[246:247]
	v_lshl_add_u64 v[246:247], v[246:247], 0, v[132:133]
	v_lshl_add_u64 v[244:245], v[246:247], 2, s[36:37]
	global_load_dwordx4 v[212:215], v[244:245], off
	global_load_dwordx4 v[216:219], v[244:245], off offset:64
	global_load_dwordx4 v[220:223], v[244:245], off offset:512
	global_load_dwordx4 v[224:227], v[244:245], off offset:576
	v_pk_mul_f32 v[108:109], v[248:249], v[108:109] op_sel_hi:[0,1]
	v_pk_mul_f32 v[110:111], v[248:249], v[110:111] op_sel_hi:[0,1]
	v_pk_fma_f32 v[110:111], v[124:125], v[110:111], v[230:231]
	v_pk_fma_f32 v[108:109], v[126:127], v[108:109], v[228:229]
	v_pk_mul_f32 v[104:105], v[248:249], v[104:105] op_sel_hi:[0,1]
	v_cvt_pk_bf16_f32 v108, v108, v109
	v_cvt_pk_bf16_f32 v109, v110, v111
	global_store_dwordx2 v[158:159], v[108:109], off
	v_pk_mul_f32 v[106:107], v[248:249], v[106:107] op_sel_hi:[0,1]
	v_pk_mul_f32 v[100:101], v[248:249], v[100:101] op_sel_hi:[0,1]
	v_pk_mul_f32 v[102:103], v[248:249], v[102:103] op_sel_hi:[0,1]
	v_pk_mul_f32 v[96:97], v[248:249], v[96:97] op_sel_hi:[0,1]
	v_pk_mul_f32 v[98:99], v[248:249], v[98:99] op_sel_hi:[0,1]
	v_pk_fma_f32 v[106:107], v[120:121], v[106:107], v[234:235]
	v_pk_fma_f32 v[104:105], v[122:123], v[104:105], v[232:233]
	s_nop 0
	v_cvt_pk_bf16_f32 v104, v104, v105
	v_cvt_pk_bf16_f32 v105, v106, v107
	global_store_dwordx2 v[158:159], v[104:105], off offset:32
	v_pk_fma_f32 v[102:103], v[116:117], v[102:103], v[238:239]
	v_pk_fma_f32 v[100:101], v[118:119], v[100:101], v[236:237]
	v_or_b32_e32 v104, 32, v134
	v_cvt_pk_bf16_f32 v100, v100, v101
	v_cvt_pk_bf16_f32 v101, v102, v103
	global_store_dwordx2 v[158:159], v[100:101], off offset:256
	v_ashrrev_i32_e32 v105, 31, v104
	v_lshl_add_u64 v[106:107], v[104:105], 2, s[14:15]
	v_lshlrev_b64 v[104:105], 11, v[104:105]
	v_lshl_add_u64 v[104:105], v[104:105], 0, v[132:133]
	v_pk_fma_f32 v[98:99], v[112:113], v[98:99], v[242:243]
	v_pk_fma_f32 v[96:97], v[114:115], v[96:97], v[240:241]
	v_lshl_add_u64 v[102:103], v[104:105], 2, s[36:37]
	v_cvt_pk_bf16_f32 v96, v96, v97
	v_cvt_pk_bf16_f32 v97, v98, v99
	global_store_dwordx2 v[158:159], v[96:97], off offset:288
	v_lshl_add_u64 v[104:105], v[104:105], 1, s[12:13]
	global_load_dword v248, v[128:129], off offset:192
	v_or_b32_e32 v246, 48, v134
	v_ashrrev_i32_e32 v247, 31, v246
	v_lshlrev_b64 v[246:247], 11, v[246:247]
	v_lshl_add_u64 v[246:247], v[246:247], 0, v[132:133]
	v_lshl_add_u64 v[244:245], v[246:247], 2, s[36:37]
	global_load_dwordx4 v[228:231], v[244:245], off
	global_load_dwordx4 v[232:235], v[244:245], off offset:64
	global_load_dwordx4 v[236:239], v[244:245], off offset:512
	global_load_dwordx4 v[240:243], v[244:245], off offset:576
	s_waitcnt vmcnt(13)
; DI unsigned pk2(float a, float b) { f32x2 f = {a, b}; bf16x2_t h = __builtin_convertvector(f, bf16x2_t); return __builtin_bit_cast(unsigned, h); }
;     __device__ __forceinline__ void operator()(const f32x4 (&acc)[2][2][4][2], const Unit& u, int wr, int wc, int fr, int fq) const {
;     ...
;         for (int ai = 0; ai < 2; ++ai)
; #pragma unroll
;             for (int m = 0; m < 4; ++m) { const int row = row0 + ai * HALF + m * 16; const float sr = asc[row]; const size_t off = (size_t)row * D + col0;
; #pragma unroll
;                 for (int bj = 0; bj < 2; ++bj)
; #pragma unroll
;                     for (int n = 0; n < 2; ++n) { const f32x4 xv = *(const f32x4*)(x + off + bj * HALF + n * 16); const f32x4 r = xv + gv[bj][n] * (__builtin_convertvector(__builtin_bit_cast(i32x4_t, acc[ai][bj][m][n]), f32x4) * sr);
;                         u32x2 w; w.x = pk2(r[0], r[1]); w.y = pk2(r[2], r[3]); *(u32x2*)(x1 + off + bj * HALF + n * 16) = w; } }
	v_pk_mul_f32 v[92:93], v[250:251], v[92:93] op_sel_hi:[0,1]
	v_pk_mul_f32 v[94:95], v[250:251], v[94:95] op_sel_hi:[0,1]
	s_waitcnt vmcnt(12)
	v_pk_fma_f32 v[94:95], v[124:125], v[94:95], v[214:215]
	v_pk_fma_f32 v[92:93], v[126:127], v[92:93], v[212:213]
	v_pk_mul_f32 v[88:89], v[250:251], v[88:89] op_sel_hi:[0,1]
	v_cvt_pk_bf16_f32 v92, v92, v93
	v_cvt_pk_bf16_f32 v93, v94, v95
	global_store_dwordx2 v[104:105], v[92:93], off
	v_pk_mul_f32 v[90:91], v[250:251], v[90:91] op_sel_hi:[0,1]
	v_pk_mul_f32 v[84:85], v[250:251], v[84:85] op_sel_hi:[0,1]
	v_pk_mul_f32 v[86:87], v[250:251], v[86:87] op_sel_hi:[0,1]
	v_pk_mul_f32 v[80:81], v[250:251], v[80:81] op_sel_hi:[0,1]
	v_pk_mul_f32 v[82:83], v[250:251], v[82:83] op_sel_hi:[0,1]
	s_waitcnt vmcnt(12)
	v_pk_fma_f32 v[90:91], v[120:121], v[90:91], v[218:219]
	v_pk_fma_f32 v[88:89], v[122:123], v[88:89], v[216:217]
	s_nop 0
	v_cvt_pk_bf16_f32 v88, v88, v89
	v_cvt_pk_bf16_f32 v89, v90, v91
	global_store_dwordx2 v[104:105], v[88:89], off offset:32
	s_waitcnt vmcnt(12)
	v_pk_fma_f32 v[86:87], v[116:117], v[86:87], v[222:223]
	v_pk_fma_f32 v[84:85], v[118:119], v[84:85], v[220:221]
	v_or_b32_e32 v88, 48, v134
	v_cvt_pk_bf16_f32 v84, v84, v85
	v_cvt_pk_bf16_f32 v85, v86, v87
	global_store_dwordx2 v[104:105], v[84:85], off offset:256
	v_ashrrev_i32_e32 v89, 31, v88
	v_lshl_add_u64 v[90:91], v[88:89], 2, s[14:15]
	v_lshlrev_b64 v[88:89], 11, v[88:89]
	v_lshl_add_u64 v[88:89], v[88:89], 0, v[132:133]
	s_waitcnt vmcnt(12)
	v_pk_fma_f32 v[82:83], v[112:113], v[82:83], v[226:227]
	v_pk_fma_f32 v[80:81], v[114:115], v[80:81], v[224:225]
	v_lshl_add_u64 v[86:87], v[88:89], 2, s[36:37]
	v_cvt_pk_bf16_f32 v80, v80, v81
	v_cvt_pk_bf16_f32 v81, v82, v83
	global_store_dwordx2 v[104:105], v[80:81], off offset:288
	v_lshl_add_u64 v[88:89], v[88:89], 1, s[12:13]
	global_load_dword v250, v[128:129], off offset:512
	v_lshl_add_u64 v[246:247], v[130:131], 0, s[22:23]
	v_lshl_add_u64 v[244:245], v[246:247], 2, s[36:37]
	global_load_dwordx4 v[212:215], v[244:245], off
	global_load_dwordx4 v[216:219], v[244:245], off offset:64
	global_load_dwordx4 v[220:223], v[244:245], off offset:512
	global_load_dwordx4 v[224:227], v[244:245], off offset:576
	s_waitcnt vmcnt(13)
	v_pk_mul_f32 v[76:77], v[248:249], v[76:77] op_sel_hi:[0,1]
	v_pk_mul_f32 v[78:79], v[248:249], v[78:79] op_sel_hi:[0,1]
	s_waitcnt vmcnt(12)
	v_pk_fma_f32 v[78:79], v[124:125], v[78:79], v[230:231]
	v_pk_fma_f32 v[76:77], v[126:127], v[76:77], v[228:229]
	v_pk_mul_f32 v[72:73], v[248:249], v[72:73] op_sel_hi:[0,1]
	v_cvt_pk_bf16_f32 v76, v76, v77
	v_cvt_pk_bf16_f32 v77, v78, v79
	global_store_dwordx2 v[88:89], v[76:77], off
	v_pk_mul_f32 v[74:75], v[248:249], v[74:75] op_sel_hi:[0,1]
	v_pk_mul_f32 v[68:69], v[248:249], v[68:69] op_sel_hi:[0,1]
	v_pk_mul_f32 v[70:71], v[248:249], v[70:71] op_sel_hi:[0,1]
	v_pk_mul_f32 v[64:65], v[248:249], v[64:65] op_sel_hi:[0,1]
	v_pk_mul_f32 v[66:67], v[248:249], v[66:67] op_sel_hi:[0,1]
	s_waitcnt vmcnt(12)
	v_pk_fma_f32 v[74:75], v[120:121], v[74:75], v[234:235]
	v_pk_fma_f32 v[72:73], v[122:123], v[72:73], v[232:233]
	s_nop 0
	v_cvt_pk_bf16_f32 v72, v72, v73
	v_cvt_pk_bf16_f32 v73, v74, v75
	global_store_dwordx2 v[88:89], v[72:73], off offset:32
	s_waitcnt vmcnt(12)
	v_pk_fma_f32 v[70:71], v[116:117], v[70:71], v[238:239]
	v_pk_fma_f32 v[68:69], v[118:119], v[68:69], v[236:237]
	v_lshl_add_u64 v[72:73], v[130:131], 0, s[22:23]
	v_cvt_pk_bf16_f32 v68, v68, v69
	v_cvt_pk_bf16_f32 v69, v70, v71
	global_store_dwordx2 v[88:89], v[68:69], off offset:256
	s_waitcnt vmcnt(12)
	v_pk_fma_f32 v[66:67], v[112:113], v[66:67], v[242:243]
	v_pk_fma_f32 v[64:65], v[114:115], v[64:65], v[240:241]
	v_lshl_add_u64 v[70:71], v[72:73], 2, s[36:37]
	v_cvt_pk_bf16_f32 v64, v64, v65
	v_cvt_pk_bf16_f32 v65, v66, v67
	global_store_dwordx2 v[88:89], v[64:65], off offset:288
	v_lshl_add_u64 v[72:73], v[72:73], 1, s[12:13]
	global_load_dword v248, v[128:129], off offset:576
	v_lshl_add_u64 v[246:247], v[130:131], 0, s[38:39]
	v_lshl_add_u64 v[244:245], v[246:247], 2, s[36:37]
	global_load_dwordx4 v[228:231], v[244:245], off
	global_load_dwordx4 v[232:235], v[244:245], off offset:64
	global_load_dwordx4 v[236:239], v[244:245], off offset:512
	global_load_dwordx4 v[240:243], v[244:245], off offset:576
	s_waitcnt vmcnt(13)
	v_pk_mul_f32 v[60:61], v[250:251], v[60:61] op_sel_hi:[0,1]
	v_pk_mul_f32 v[62:63], v[250:251], v[62:63] op_sel_hi:[0,1]
	s_waitcnt vmcnt(12)
	v_pk_fma_f32 v[62:63], v[124:125], v[62:63], v[214:215]
	v_pk_fma_f32 v[60:61], v[126:127], v[60:61], v[212:213]
	v_pk_mul_f32 v[56:57], v[250:251], v[56:57] op_sel_hi:[0,1]
	v_cvt_pk_bf16_f32 v60, v60, v61
	v_cvt_pk_bf16_f32 v61, v62, v63
	global_store_dwordx2 v[72:73], v[60:61], off
	v_pk_mul_f32 v[58:59], v[250:251], v[58:59] op_sel_hi:[0,1]
	v_pk_mul_f32 v[52:53], v[250:251], v[52:53] op_sel_hi:[0,1]
	v_pk_mul_f32 v[54:55], v[250:251], v[54:55] op_sel_hi:[0,1]
	v_pk_mul_f32 v[48:49], v[250:251], v[48:49] op_sel_hi:[0,1]
	v_pk_mul_f32 v[50:51], v[250:251], v[50:51] op_sel_hi:[0,1]
	s_waitcnt vmcnt(12)
	v_pk_fma_f32 v[58:59], v[120:121], v[58:59], v[218:219]
	v_pk_fma_f32 v[56:57], v[122:123], v[56:57], v[216:217]
	s_nop 0
	v_cvt_pk_bf16_f32 v56, v56, v57
	v_cvt_pk_bf16_f32 v57, v58, v59
	global_store_dwordx2 v[72:73], v[56:57], off offset:32
	s_waitcnt vmcnt(12)
	v_pk_fma_f32 v[54:55], v[116:117], v[54:55], v[222:223]
	v_pk_fma_f32 v[52:53], v[118:119], v[52:53], v[220:221]
	v_lshl_add_u64 v[56:57], v[130:131], 0, s[38:39]
	v_cvt_pk_bf16_f32 v52, v52, v53
	v_cvt_pk_bf16_f32 v53, v54, v55
	global_store_dwordx2 v[72:73], v[52:53], off offset:256
	s_waitcnt vmcnt(12)
; DI unsigned pk2(float a, float b) { f32x2 f = {a, b}; bf16x2_t h = __builtin_convertvector(f, bf16x2_t); return __builtin_bit_cast(unsigned, h); }
;     __device__ __forceinline__ void operator()(const f32x4 (&acc)[2][2][4][2], const Unit& u, int wr, int wc, int fr, int fq) const {
;     ...
;         for (int ai = 0; ai < 2; ++ai)
; #pragma unroll
;             for (int m = 0; m < 4; ++m) { const int row = row0 + ai * HALF + m * 16; const float sr = asc[row]; const size_t off = (size_t)row * D + col0;
; #pragma unroll
;                 for (int bj = 0; bj < 2; ++bj)
; #pragma unroll
;                     for (int n = 0; n < 2; ++n) { const f32x4 xv = *(const f32x4*)(x + off + bj * HALF + n * 16); const f32x4 r = xv + gv[bj][n] * (__builtin_convertvector(__builtin_bit_cast(i32x4_t, acc[ai][bj][m][n]), f32x4) * sr);
;                         u32x2 w; w.x = pk2(r[0], r[1]); w.y = pk2(r[2], r[3]); *(u32x2*)(x1 + off + bj * HALF + n * 16) = w; } }
	v_pk_fma_f32 v[50:51], v[112:113], v[50:51], v[226:227]
	v_pk_fma_f32 v[48:49], v[114:115], v[48:49], v[224:225]
	v_lshl_add_u64 v[54:55], v[56:57], 2, s[36:37]
	v_cvt_pk_bf16_f32 v48, v48, v49
	v_cvt_pk_bf16_f32 v49, v50, v51
	global_store_dwordx2 v[72:73], v[48:49], off offset:288
	v_lshl_add_u64 v[56:57], v[56:57], 1, s[12:13]
	global_load_dword v250, v[128:129], off offset:640
	v_lshl_add_u64 v[246:247], v[130:131], 0, s[40:41]
	v_lshl_add_u64 v[244:245], v[246:247], 2, s[36:37]
	global_load_dwordx4 v[212:215], v[244:245], off
	global_load_dwordx4 v[216:219], v[244:245], off offset:64
	global_load_dwordx4 v[220:223], v[244:245], off offset:512
	global_load_dwordx4 v[224:227], v[244:245], off offset:576
	s_waitcnt vmcnt(13)
	v_pk_mul_f32 v[44:45], v[248:249], v[44:45] op_sel_hi:[0,1]
	v_pk_mul_f32 v[46:47], v[248:249], v[46:47] op_sel_hi:[0,1]
	s_waitcnt vmcnt(12)
	v_pk_fma_f32 v[46:47], v[124:125], v[46:47], v[230:231]
	v_pk_fma_f32 v[44:45], v[126:127], v[44:45], v[228:229]
	v_pk_mul_f32 v[40:41], v[248:249], v[40:41] op_sel_hi:[0,1]
	v_cvt_pk_bf16_f32 v44, v44, v45
	v_cvt_pk_bf16_f32 v45, v46, v47
	global_store_dwordx2 v[56:57], v[44:45], off
	v_pk_mul_f32 v[42:43], v[248:249], v[42:43] op_sel_hi:[0,1]
	v_pk_mul_f32 v[36:37], v[248:249], v[36:37] op_sel_hi:[0,1]
	v_pk_mul_f32 v[38:39], v[248:249], v[38:39] op_sel_hi:[0,1]
	v_pk_mul_f32 v[32:33], v[248:249], v[32:33] op_sel_hi:[0,1]
	v_pk_mul_f32 v[34:35], v[248:249], v[34:35] op_sel_hi:[0,1]
	s_waitcnt vmcnt(12)
	v_pk_fma_f32 v[42:43], v[120:121], v[42:43], v[234:235]
	v_pk_fma_f32 v[40:41], v[122:123], v[40:41], v[232:233]
	s_nop 0
	v_cvt_pk_bf16_f32 v40, v40, v41
	v_cvt_pk_bf16_f32 v41, v42, v43
	global_store_dwordx2 v[56:57], v[40:41], off offset:32
	s_waitcnt vmcnt(12)
	v_pk_fma_f32 v[38:39], v[116:117], v[38:39], v[238:239]
	v_pk_fma_f32 v[36:37], v[118:119], v[36:37], v[236:237]
	v_lshl_add_u64 v[40:41], v[130:131], 0, s[40:41]
	v_cvt_pk_bf16_f32 v36, v36, v37
	v_cvt_pk_bf16_f32 v37, v38, v39
	global_store_dwordx2 v[56:57], v[36:37], off offset:256
	s_waitcnt vmcnt(12)
	v_pk_fma_f32 v[34:35], v[112:113], v[34:35], v[242:243]
	v_pk_fma_f32 v[32:33], v[114:115], v[32:33], v[240:241]
	v_lshl_add_u64 v[38:39], v[40:41], 2, s[36:37]
	v_cvt_pk_bf16_f32 v32, v32, v33
	v_cvt_pk_bf16_f32 v33, v34, v35
	global_store_dwordx2 v[56:57], v[32:33], off offset:288
	v_lshl_add_u64 v[40:41], v[40:41], 1, s[12:13]
	global_load_dword v248, v[128:129], off offset:704
	v_lshl_add_u64 v[246:247], v[130:131], 0, s[42:43]
	v_lshl_add_u64 v[244:245], v[246:247], 2, s[36:37]
	global_load_dwordx4 v[228:231], v[244:245], off
	global_load_dwordx4 v[232:235], v[244:245], off offset:64
	global_load_dwordx4 v[236:239], v[244:245], off offset:512
	global_load_dwordx4 v[240:243], v[244:245], off offset:576
	s_waitcnt vmcnt(13)
	v_pk_mul_f32 v[28:29], v[250:251], v[28:29] op_sel_hi:[0,1]
	v_pk_mul_f32 v[30:31], v[250:251], v[30:31] op_sel_hi:[0,1]
	s_waitcnt vmcnt(12)
	v_pk_fma_f32 v[30:31], v[124:125], v[30:31], v[214:215]
	v_pk_fma_f32 v[28:29], v[126:127], v[28:29], v[212:213]
	v_pk_mul_f32 v[24:25], v[250:251], v[24:25] op_sel_hi:[0,1]
	v_cvt_pk_bf16_f32 v28, v28, v29
	v_cvt_pk_bf16_f32 v29, v30, v31
	global_store_dwordx2 v[40:41], v[28:29], off
	v_pk_mul_f32 v[26:27], v[250:251], v[26:27] op_sel_hi:[0,1]
	v_pk_mul_f32 v[20:21], v[250:251], v[20:21] op_sel_hi:[0,1]
	v_pk_mul_f32 v[22:23], v[250:251], v[22:23] op_sel_hi:[0,1]
	v_pk_mul_f32 v[16:17], v[250:251], v[16:17] op_sel_hi:[0,1]
	v_pk_mul_f32 v[18:19], v[250:251], v[18:19] op_sel_hi:[0,1]
	s_waitcnt vmcnt(12)
	v_pk_fma_f32 v[26:27], v[120:121], v[26:27], v[218:219]
	v_pk_fma_f32 v[24:25], v[122:123], v[24:25], v[216:217]
	s_nop 0
	v_cvt_pk_bf16_f32 v24, v24, v25
	v_cvt_pk_bf16_f32 v25, v26, v27
	global_store_dwordx2 v[40:41], v[24:25], off offset:32
	s_waitcnt vmcnt(12)
	v_pk_fma_f32 v[22:23], v[116:117], v[22:23], v[222:223]
	v_pk_fma_f32 v[20:21], v[118:119], v[20:21], v[220:221]
	v_lshl_add_u64 v[24:25], v[130:131], 0, s[42:43]
	v_cvt_pk_bf16_f32 v20, v20, v21
	v_cvt_pk_bf16_f32 v21, v22, v23
	global_store_dwordx2 v[40:41], v[20:21], off offset:256
	s_waitcnt vmcnt(12)
	v_pk_fma_f32 v[18:19], v[112:113], v[18:19], v[226:227]
	v_pk_fma_f32 v[16:17], v[114:115], v[16:17], v[224:225]
	v_lshl_add_u64 v[22:23], v[24:25], 2, s[36:37]
	v_cvt_pk_bf16_f32 v16, v16, v17
	v_cvt_pk_bf16_f32 v17, v18, v19
	global_store_dwordx2 v[40:41], v[16:17], off offset:288
	v_lshl_add_u64 v[24:25], v[24:25], 1, s[12:13]
	s_waitcnt vmcnt(8)
	v_pk_mul_f32 v[12:13], v[248:249], v[12:13] op_sel_hi:[0,1]
	v_pk_mul_f32 v[14:15], v[248:249], v[14:15] op_sel_hi:[0,1]
	s_waitcnt vmcnt(7)
	v_pk_fma_f32 v[14:15], v[124:125], v[14:15], v[230:231]
	v_pk_fma_f32 v[12:13], v[126:127], v[12:13], v[228:229]
	v_pk_mul_f32 v[8:9], v[248:249], v[8:9] op_sel_hi:[0,1]
	v_cvt_pk_bf16_f32 v12, v12, v13
	v_cvt_pk_bf16_f32 v13, v14, v15
	global_store_dwordx2 v[24:25], v[12:13], off
	v_pk_mul_f32 v[10:11], v[248:249], v[10:11] op_sel_hi:[0,1]
	v_pk_mul_f32 v[4:5], v[248:249], v[4:5] op_sel_hi:[0,1]
	v_pk_mul_f32 v[6:7], v[248:249], v[6:7] op_sel_hi:[0,1]
	v_pk_mul_f32 v[0:1], v[248:249], v[0:1] op_sel_hi:[0,1]
	v_pk_mul_f32 v[2:3], v[248:249], v[2:3] op_sel_hi:[0,1]
	s_waitcnt vmcnt(7)
	v_pk_fma_f32 v[10:11], v[120:121], v[10:11], v[234:235]
	v_pk_fma_f32 v[8:9], v[122:123], v[8:9], v[232:233]
	s_nop 0
	v_cvt_pk_bf16_f32 v8, v8, v9
	v_cvt_pk_bf16_f32 v9, v10, v11
	global_store_dwordx2 v[24:25], v[8:9], off offset:32
	s_waitcnt vmcnt(7)
	v_pk_fma_f32 v[6:7], v[116:117], v[6:7], v[238:239]
	v_pk_fma_f32 v[4:5], v[118:119], v[4:5], v[236:237]
	s_nop 0
	v_cvt_pk_bf16_f32 v4, v4, v5
	v_cvt_pk_bf16_f32 v5, v6, v7
	global_store_dwordx2 v[24:25], v[4:5], off offset:256
	s_waitcnt vmcnt(7)
	v_pk_fma_f32 v[2:3], v[112:113], v[2:3], v[242:243]
	v_pk_fma_f32 v[0:1], v[114:115], v[0:1], v[240:241]
	s_nop 0
	v_cvt_pk_bf16_f32 v0, v0, v1
	v_cvt_pk_bf16_f32 v1, v2, v3
	global_store_dwordx2 v[24:25], v[0:1], off offset:288
	s_cbranch_vccnz .LBB0_951
	s_andn2_b64 vcc, exec, s[10:11]
	s_cbranch_vccnz .LBB0_950
	s_barrier
	s_branch .LBB0_950
